# v30 + grid barrier acquire: the L1 invalidate (buffer_inv sc1) is issued at arrival, overlapped with the arrival atomic / wait, instead of after the release (no loads enter L1 while the workgroup wait
# speedup vs baseline: 1.0074x; 1.0074x over previous
.LBB0_90:
	s_mov_b64 s[6:7], exec
	v_readlane_b32 s4, v254, 8
	s_lshl_b32 s4, s4, 8
	v_readlane_b32 s8, v254, 6
	v_mbcnt_lo_u32_b32 v2, s6, 0
	v_readlane_b32 s9, v254, 7
	s_add_u32 s4, s8, s4
	v_mbcnt_hi_u32_b32 v2, s7, v2
	s_addc_u32 s5, s9, 0
	v_cmp_eq_u32_e32 vcc, 0, v2
	s_and_saveexec_b64 s[8:9], vcc
	s_cbranch_execz .LBB0_92
	s_bcnt1_i32_b64 s6, s[6:7]
	v_mov_b32_e32 v4, 0x1000
	v_mov_b32_e32 v5, s6
	buffer_inv sc1
	global_atomic_add v4, v4, v5, s[4:5] offset:1024 sc0

.LBB0_105:
	s_or_b64 exec, exec, s[8:9]
	s_waitcnt vmcnt(0)
	s_waitcnt vmcnt(0)

.LBB0_123:
	s_or_b64 exec, exec, s[6:7]
	s_mov_b64 s[6:7], exec
	v_mbcnt_lo_u32_b32 v1, s6, 0
	v_mbcnt_hi_u32_b32 v1, s7, v1
	v_cmp_eq_u32_e32 vcc, 0, v1
	s_waitcnt vmcnt(0)
	s_and_saveexec_b64 s[8:9], vcc
	s_cbranch_execz .LBB0_125
	s_bcnt1_i32_b64 s6, s[6:7]
	v_mov_b32_e32 v1, 0x2000
	v_mov_b32_e32 v2, s6
	global_atomic_add v1, v2, s[4:5] offset:1024

.LBB0_2023:
	s_mov_b64 s[6:7], exec
	v_readlane_b32 s4, v254, 8
	s_lshl_b32 s4, s4, 8
	v_readlane_b32 s8, v254, 6
	v_mbcnt_lo_u32_b32 v1, s6, 0
	v_readlane_b32 s9, v254, 7
	s_add_u32 s4, s8, s4
	v_mbcnt_hi_u32_b32 v1, s7, v1
	s_addc_u32 s5, s9, 0
	v_cmp_eq_u32_e32 vcc, 0, v1
	s_and_saveexec_b64 s[8:9], vcc
	s_cbranch_execz .LBB0_2025
	s_bcnt1_i32_b64 s6, s[6:7]
	v_mov_b32_e32 v3, 0x1000
	v_mov_b32_e32 v4, s6
	buffer_inv sc1
	global_atomic_add v3, v3, v4, s[4:5] offset:1024 sc0

.LBB0_2056:
	s_or_b64 exec, exec, s[6:7]
	s_mov_b64 s[6:7], exec
	v_mbcnt_lo_u32_b32 v0, s6, 0
	v_mbcnt_hi_u32_b32 v0, s7, v0
	v_cmp_eq_u32_e32 vcc, 0, v0
	s_waitcnt vmcnt(0)
	s_and_saveexec_b64 s[8:9], vcc
	s_cbranch_execz .LBB0_2058
	s_bcnt1_i32_b64 s6, s[6:7]
	v_mov_b32_e32 v0, 0x2000
	v_mov_b32_e32 v1, s6
	global_atomic_add v0, v1, s[4:5] offset:1024
